# previous stack + fp8 GEMM epilogue hazard padding trimmed to 32 wait states
# baseline (speedup 1.0000x reference)
; __device__ __forceinline__ unsigned cvt_pk_bf16(float lo, float hi) { unsigned r; asm volatile("v_cvt_pk_bf16_f32 %0, %1, %2" : "=v"(r) : "v"(lo), "v"(hi)); return r; }
; template <class Epi, class Sched, bool ALIGN_EPI, bool FP8 = false>
; __device__ __forceinline__ void gemm_phase(PG8_LAS unsigned char* lds, const Gemm g, const Sched& S, const Epi& E, const int wid, const int lane) {
;     ...
;         if constexpr (FP8) {
; #pragma unroll
;             for (int a = 0; a < 2; ++a)
; #pragma unroll
;                 for (int b = 0; b < 2; ++b) asm volatile("s_nop 15\n\ts_nop 15" : "+v"(acc[a][b][0][0]), "+v"(acc[a][b][0][1]), "+v"(acc[a][b][1][0]), "+v"(acc[a][b][1][1]), "+v"(acc[a][b][2][0]), "+v"(acc[a][b][2][1]), "+v"(acc[a][b][3][0]), "+v"(acc[a][b][3][1]));
;         }
;         E(acc, cur, wr, wc, fr, fq);
;         if (!has_next) break;
;     __device__ __forceinline__ void operator()(const f32x4 (&acc)[2][2][4][2], const Unit& u, int wr, int wc, int fr, int fq) const {
;         const int row0 = u.pm * BM + wr * 64 + fr, col0 = u.pn * BM + wc * 32 + 8 * fq;
; #pragma unroll
;         for (int ai = 0; ai < 2; ++ai)
; #pragma unroll
;             for (int m = 0; m < 4; ++m) { bf16* rowp = O + (size_t)(row0 + ai * HALF + m * 16) * D + col0;
; #pragma unroll
;                 for (int bj = 0; bj < 2; ++bj) { const f32x4 v0 = acc[ai][bj][m][0], v1 = acc[ai][bj][m][1];
;                     pg8::u32x4 w; w.x = cvt_pk_bf16(v0[0], v0[1]); w.y = cvt_pk_bf16(v0[2], v0[3]); w.z = cvt_pk_bf16(v1[0], v1[1]); w.w = cvt_pk_bf16(v1[2], v1[3]);
;                     *(pg8::u32x4*)(rowp + bj * HALF) = w; } }
;     }
.LBB0_547:
	v_lshl_add_u32 v6, s83, 8, v161
	v_lshl_add_u32 v0, s84, 8, v163
	v_ashrrev_i32_e32 v7, 31, v6
	v_ashrrev_i32_e32 v1, 31, v0
	v_lshlrev_b64 v[2:3], 12, v[6:7]
	v_lshl_add_u64 v[2:3], s[12:13], 0, v[2:3]
	v_lshlrev_b64 v[8:9], 1, v[0:1]
	s_nop 15
	s_nop 15
	v_lshl_add_u64 v[0:1], v[2:3], 0, v[8:9]
	v_cvt_pk_bf16_f32 v2, v156, v157
	v_cvt_pk_bf16_f32 v3, v158, v159
	v_cvt_pk_bf16_f32 v4, v152, v153
	v_cvt_pk_bf16_f32 v5, v154, v155
	global_store_dwordx4 v[0:1], v[2:5], off
	s_nop 1
	v_cvt_pk_bf16_f32 v2, v148, v149
	v_cvt_pk_bf16_f32 v3, v150, v151
	v_cvt_pk_bf16_f32 v4, v144, v145
	v_cvt_pk_bf16_f32 v5, v146, v147
	global_store_dwordx4 v[0:1], v[2:5], off offset:256
	s_nop 1
	v_or_b32_e32 v2, 16, v6
	v_ashrrev_i32_e32 v3, 31, v2
	v_lshlrev_b64 v[2:3], 12, v[2:3]
	v_lshl_add_u64 v[2:3], s[12:13], 0, v[2:3]
	v_lshl_add_u64 v[10:11], v[2:3], 0, v[8:9]
	v_cvt_pk_bf16_f32 v2, v140, v141
	v_cvt_pk_bf16_f32 v3, v142, v143
	v_cvt_pk_bf16_f32 v4, v136, v137
	v_cvt_pk_bf16_f32 v5, v138, v139
	global_store_dwordx4 v[10:11], v[2:5], off
	s_nop 1
	v_cvt_pk_bf16_f32 v2, v132, v133
	v_cvt_pk_bf16_f32 v3, v134, v135
	v_cvt_pk_bf16_f32 v4, v128, v129
	v_cvt_pk_bf16_f32 v5, v130, v131
	global_store_dwordx4 v[10:11], v[2:5], off offset:256
	s_nop 1
	v_or_b32_e32 v2, 32, v6
	v_ashrrev_i32_e32 v3, 31, v2
	v_lshlrev_b64 v[2:3], 12, v[2:3]
	v_lshl_add_u64 v[2:3], s[12:13], 0, v[2:3]
	v_lshl_add_u64 v[10:11], v[2:3], 0, v[8:9]
	v_cvt_pk_bf16_f32 v2, v124, v125
	v_cvt_pk_bf16_f32 v3, v126, v127
	v_cvt_pk_bf16_f32 v4, v120, v121
	v_cvt_pk_bf16_f32 v5, v122, v123
	global_store_dwordx4 v[10:11], v[2:5], off
	s_nop 1
	v_cvt_pk_bf16_f32 v2, v116, v117
	v_cvt_pk_bf16_f32 v3, v118, v119
	v_cvt_pk_bf16_f32 v4, v112, v113
	v_cvt_pk_bf16_f32 v5, v114, v115
	global_store_dwordx4 v[10:11], v[2:5], off offset:256
	s_nop 1
	v_or_b32_e32 v2, 48, v6
	v_ashrrev_i32_e32 v3, 31, v2
	v_lshlrev_b64 v[2:3], 12, v[2:3]
	v_lshl_add_u64 v[2:3], s[12:13], 0, v[2:3]
	v_lshl_add_u64 v[6:7], v[2:3], 0, v[8:9]
	v_cvt_pk_bf16_f32 v2, v108, v109
	v_cvt_pk_bf16_f32 v3, v110, v111
	v_cvt_pk_bf16_f32 v4, v104, v105
	v_cvt_pk_bf16_f32 v5, v106, v107
	global_store_dwordx4 v[6:7], v[2:5], off
	v_add_co_u32_e32 v8, vcc, s70, v0
	s_nop 0
	v_cvt_pk_bf16_f32 v2, v100, v101
	v_cvt_pk_bf16_f32 v3, v102, v103
	v_cvt_pk_bf16_f32 v4, v96, v97
	v_cvt_pk_bf16_f32 v5, v98, v99
	global_store_dwordx4 v[6:7], v[2:5], off offset:256
	v_addc_co_u32_e32 v9, vcc, 0, v1, vcc
	s_nop 0
	v_cvt_pk_bf16_f32 v2, v92, v93
	v_cvt_pk_bf16_f32 v3, v94, v95
	v_cvt_pk_bf16_f32 v4, v88, v89
	v_cvt_pk_bf16_f32 v5, v90, v91
	v_lshl_add_u64 v[6:7], v[0:1], 0, s[18:19]
	global_store_dwordx4 v[8:9], v[2:5], off
	v_add_co_u32_e32 v8, vcc, s71, v0
	s_nop 0
	v_cvt_pk_bf16_f32 v2, v84, v85
	v_cvt_pk_bf16_f32 v3, v86, v87
	v_cvt_pk_bf16_f32 v4, v80, v81
	v_cvt_pk_bf16_f32 v5, v82, v83
	global_store_dwordx4 v[6:7], v[2:5], off offset:256
	v_addc_co_u32_e32 v9, vcc, 0, v1, vcc
	s_nop 0
	v_cvt_pk_bf16_f32 v2, v76, v77
	v_cvt_pk_bf16_f32 v3, v78, v79
	v_cvt_pk_bf16_f32 v4, v72, v73
	v_cvt_pk_bf16_f32 v5, v74, v75
	v_lshl_add_u64 v[6:7], v[0:1], 0, s[20:21]
	global_store_dwordx4 v[8:9], v[2:5], off
	v_add_co_u32_e32 v8, vcc, s72, v0
	s_nop 0
	v_cvt_pk_bf16_f32 v2, v68, v69
	v_cvt_pk_bf16_f32 v3, v70, v71
	v_cvt_pk_bf16_f32 v4, v64, v65
	v_cvt_pk_bf16_f32 v5, v66, v67
	global_store_dwordx4 v[6:7], v[2:5], off offset:256
	v_lshl_add_u64 v[6:7], v[0:1], 0, s[22:23]
	v_addc_co_u32_e32 v9, vcc, 0, v1, vcc
	v_cvt_pk_bf16_f32 v2, v60, v61
	v_cvt_pk_bf16_f32 v3, v62, v63
	v_cvt_pk_bf16_f32 v4, v56, v57
	v_cvt_pk_bf16_f32 v5, v58, v59
	global_store_dwordx4 v[8:9], v[2:5], off
	s_nop 1
	v_cvt_pk_bf16_f32 v2, v52, v53
	v_cvt_pk_bf16_f32 v3, v54, v55
	v_cvt_pk_bf16_f32 v4, v48, v49
	v_cvt_pk_bf16_f32 v5, v50, v51
	global_store_dwordx4 v[6:7], v[2:5], off offset:256
	v_lshl_add_u64 v[6:7], v[0:1], 0, s[24:25]
	v_add_co_u32_e32 v0, vcc, s73, v0
	v_cvt_pk_bf16_f32 v2, v44, v45
	v_cvt_pk_bf16_f32 v3, v46, v47
	v_cvt_pk_bf16_f32 v4, v40, v41
	v_cvt_pk_bf16_f32 v5, v42, v43
	s_nop 1
	v_addc_co_u32_e32 v1, vcc, 0, v1, vcc
	s_and_b64 vcc, exec, s[0:1]
	s_mov_b64 s[0:1], -1
	global_store_dwordx4 v[0:1], v[2:5], off
	v_cvt_pk_bf16_f32 v0, v36, v37
	v_cvt_pk_bf16_f32 v1, v38, v39
	s_nop 1
	v_cvt_pk_bf16_f32 v2, v32, v33
	v_cvt_pk_bf16_f32 v3, v34, v35
	global_store_dwordx4 v[6:7], v[0:3], off offset:256
	s_cbranch_vccnz .LBB0_531
	s_andn2_b64 vcc, exec, s[10:11]
	s_cbranch_vccnz .LBB0_530
	s_barrier
	s_branch .LBB0_530

; template <class Epi, class Sched, bool ALIGN_EPI, bool FP8 = false>
; __device__ __forceinline__ void gemm_phase(PG8_LAS unsigned char* lds, const Gemm g, const Sched& S, const Epi& E, const int wid, const int lane) {
;     ...
;         if constexpr (FP8) {
; #pragma unroll
;             for (int a = 0; a < 2; ++a)
; #pragma unroll
;                 for (int b = 0; b < 2; ++b) asm volatile("s_nop 15\n\ts_nop 15" : "+v"(acc[a][b][0][0]), "+v"(acc[a][b][0][1]), "+v"(acc[a][b][1][0]), "+v"(acc[a][b][1][1]), "+v"(acc[a][b][2][0]), "+v"(acc[a][b][2][1]), "+v"(acc[a][b][3][0]), "+v"(acc[a][b][3][1]));
;         }
;     __device__ __forceinline__ void operator()(const f32x4 (&acc)[2][2][4][2], const Unit& u, int wr, int wc, int fr, int fq) const {
;         const int col0 = (u.pn & 7) * 256 + wc * 64 + 16 * fq;
;         const int e = tileE[u.pm], lbase = (u.pm - tb[e]) * 256 + wr * 64 + fr, ce = cnt[e];
;         const float ysc = (float)(1 << YSHIFT);
;         int drow[2][4];
; #pragma unroll
;         for (int ai = 0; ai < 2; ++ai)
; #pragma unroll
;             for (int m = 0; m < 4; ++m) { const int local = lbase + ai * HALF + m * 16; drow[ai][m] = (e >= NE) ? (local * 7 + 6) : ((local < ce) ? list2[(size_t)e * LISTCAP + local] : 7 * T); }
.LBB0_855:
	s_lshl_b32 s6, s74, 2
	s_add_i32 s6, s6, 0
	s_add_i32 s6, s6, 0x20800
	v_mov_b32_e32 v0, s6
	s_nop 15
	s_nop 15
	ds_read_b32 v2, v0
	s_mov_b64 s[6:7], -1
	s_waitcnt lgkmcnt(0)
	v_lshlrev_b32_e32 v0, 2, v2
	v_add_u32_e32 v0, 0, v0
	v_add_u32_e32 v1, 0x21000, v0
	ds_read_b32 v4, v1
	v_add_u32_e32 v0, 0x21200, v0
	ds_read_b32 v1, v0
	v_ashrrev_i32_e32 v3, 31, v2
	v_cmp_gt_i64_e64 s[8:9], 64, v[2:3]
	s_waitcnt lgkmcnt(1)
	v_sub_u32_e32 v0, s74, v4
	v_lshlrev_b64 v[2:3], 16, v[2:3]
	v_lshl_add_u32 v16, v0, 8, v161
	v_lshl_add_u64 v[18:19], s[20:21], 0, v[2:3]
	s_and_b64 vcc, exec, s[8:9]
	s_cbranch_vccz .LBB0_859
	s_waitcnt lgkmcnt(0)
	v_cmp_lt_i32_e32 vcc, v16, v1
	v_mov_b32_e32 v10, 0x1c000
	s_and_saveexec_b64 s[6:7], vcc
	s_cbranch_execz .LBB0_858
	v_ashrrev_i32_e32 v17, 31, v16
	v_lshl_add_u64 v[2:3], v[16:17], 2, v[18:19]
	global_load_dword v10, v[2:3], off

; __device__ __forceinline__ unsigned cvt_pk_bf16(float lo, float hi) { unsigned r; asm volatile("v_cvt_pk_bf16_f32 %0, %1, %2" : "=v"(r) : "v"(lo), "v"(hi)); return r; }
; template <class Epi, class Sched, bool ALIGN_EPI, bool FP8 = false>
; __device__ __forceinline__ void gemm_phase(PG8_LAS unsigned char* lds, const Gemm g, const Sched& S, const Epi& E, const int wid, const int lane) {
;     ...
;         if constexpr (FP8) {
; #pragma unroll
;             for (int a = 0; a < 2; ++a)
; #pragma unroll
;                 for (int b = 0; b < 2; ++b) asm volatile("s_nop 15\n\ts_nop 15" : "+v"(acc[a][b][0][0]), "+v"(acc[a][b][0][1]), "+v"(acc[a][b][1][0]), "+v"(acc[a][b][1][1]), "+v"(acc[a][b][2][0]), "+v"(acc[a][b][2][1]), "+v"(acc[a][b][3][0]), "+v"(acc[a][b][3][1]));
;         }
;         E(acc, cur, wr, wc, fr, fq);
;         if (!has_next) break;
;     __device__ __forceinline__ void operator()(const f32x4 (&acc)[2][2][4][2], const Unit& u, int wr, int wc, int fr, int fq) const {
;         const int row0 = u.pm * BM + wr * 64 + fr, col0 = u.pn * BM + wc * 32 + 8 * fq;
; #pragma unroll
;         for (int ai = 0; ai < 2; ++ai)
; #pragma unroll
;             for (int m = 0; m < 4; ++m) { bf16* rowp = O + (size_t)(row0 + ai * HALF + m * 16) * D + col0;
; #pragma unroll
;                 for (int bj = 0; bj < 2; ++bj) { const f32x4 v0 = acc[ai][bj][m][0], v1 = acc[ai][bj][m][1];
;                     pg8::u32x4 w; w.x = cvt_pk_bf16(v0[0], v0[1]); w.y = cvt_pk_bf16(v0[2], v0[3]); w.z = cvt_pk_bf16(v1[0], v1[1]); w.w = cvt_pk_bf16(v1[2], v1[3]);
;                     *(pg8::u32x4*)(rowp + bj * HALF) = w; } }
;     }
.LBB0_1457:
	v_lshl_add_u32 v6, s82, 8, v161
	v_lshl_add_u32 v0, s83, 8, v163
	v_ashrrev_i32_e32 v7, 31, v6
	v_ashrrev_i32_e32 v1, 31, v0
	v_lshlrev_b64 v[2:3], 12, v[6:7]
	v_lshl_add_u64 v[2:3], s[12:13], 0, v[2:3]
	v_lshlrev_b64 v[8:9], 1, v[0:1]
	s_nop 15
	s_nop 15
	v_lshl_add_u64 v[0:1], v[2:3], 0, v[8:9]
	v_cvt_pk_bf16_f32 v2, v156, v157
	v_cvt_pk_bf16_f32 v3, v158, v159
	v_cvt_pk_bf16_f32 v4, v152, v153
	v_cvt_pk_bf16_f32 v5, v154, v155
	global_store_dwordx4 v[0:1], v[2:5], off
	s_nop 1
	v_cvt_pk_bf16_f32 v2, v148, v149
	v_cvt_pk_bf16_f32 v3, v150, v151
	v_cvt_pk_bf16_f32 v4, v144, v145
	v_cvt_pk_bf16_f32 v5, v146, v147
	global_store_dwordx4 v[0:1], v[2:5], off offset:256
	s_nop 1
	v_or_b32_e32 v2, 16, v6
	v_ashrrev_i32_e32 v3, 31, v2
	v_lshlrev_b64 v[2:3], 12, v[2:3]
	v_lshl_add_u64 v[2:3], s[12:13], 0, v[2:3]
	v_lshl_add_u64 v[10:11], v[2:3], 0, v[8:9]
	v_cvt_pk_bf16_f32 v2, v140, v141
	v_cvt_pk_bf16_f32 v3, v142, v143
	v_cvt_pk_bf16_f32 v4, v136, v137
	v_cvt_pk_bf16_f32 v5, v138, v139
	global_store_dwordx4 v[10:11], v[2:5], off
	s_nop 1
	v_cvt_pk_bf16_f32 v2, v132, v133
	v_cvt_pk_bf16_f32 v3, v134, v135
	v_cvt_pk_bf16_f32 v4, v128, v129
	v_cvt_pk_bf16_f32 v5, v130, v131
	global_store_dwordx4 v[10:11], v[2:5], off offset:256
	s_nop 1
	v_or_b32_e32 v2, 32, v6
	v_ashrrev_i32_e32 v3, 31, v2
	v_lshlrev_b64 v[2:3], 12, v[2:3]
	v_lshl_add_u64 v[2:3], s[12:13], 0, v[2:3]
	v_lshl_add_u64 v[10:11], v[2:3], 0, v[8:9]
	v_cvt_pk_bf16_f32 v2, v124, v125
	v_cvt_pk_bf16_f32 v3, v126, v127
	v_cvt_pk_bf16_f32 v4, v120, v121
	v_cvt_pk_bf16_f32 v5, v122, v123
	global_store_dwordx4 v[10:11], v[2:5], off
	s_nop 1
	v_cvt_pk_bf16_f32 v2, v116, v117
	v_cvt_pk_bf16_f32 v3, v118, v119
	v_cvt_pk_bf16_f32 v4, v112, v113
	v_cvt_pk_bf16_f32 v5, v114, v115
	global_store_dwordx4 v[10:11], v[2:5], off offset:256
	s_nop 1
	v_or_b32_e32 v2, 48, v6
	v_ashrrev_i32_e32 v3, 31, v2
	v_lshlrev_b64 v[2:3], 12, v[2:3]
	v_lshl_add_u64 v[2:3], s[12:13], 0, v[2:3]
	v_lshl_add_u64 v[6:7], v[2:3], 0, v[8:9]
	v_cvt_pk_bf16_f32 v2, v108, v109
	v_cvt_pk_bf16_f32 v3, v110, v111
	v_cvt_pk_bf16_f32 v4, v104, v105
	v_cvt_pk_bf16_f32 v5, v106, v107
	global_store_dwordx4 v[6:7], v[2:5], off
	v_add_co_u32_e32 v8, vcc, s70, v0
	s_nop 0
	v_cvt_pk_bf16_f32 v2, v100, v101
	v_cvt_pk_bf16_f32 v3, v102, v103
	v_cvt_pk_bf16_f32 v4, v96, v97
	v_cvt_pk_bf16_f32 v5, v98, v99
	global_store_dwordx4 v[6:7], v[2:5], off offset:256
	v_addc_co_u32_e32 v9, vcc, 0, v1, vcc
	s_nop 0
	v_cvt_pk_bf16_f32 v2, v92, v93
	v_cvt_pk_bf16_f32 v3, v94, v95
	v_cvt_pk_bf16_f32 v4, v88, v89
	v_cvt_pk_bf16_f32 v5, v90, v91
	v_lshl_add_u64 v[6:7], v[0:1], 0, s[18:19]
	global_store_dwordx4 v[8:9], v[2:5], off
	v_add_co_u32_e32 v8, vcc, s71, v0
	s_nop 0
	v_cvt_pk_bf16_f32 v2, v84, v85
	v_cvt_pk_bf16_f32 v3, v86, v87
	v_cvt_pk_bf16_f32 v4, v80, v81
	v_cvt_pk_bf16_f32 v5, v82, v83
	global_store_dwordx4 v[6:7], v[2:5], off offset:256
	v_addc_co_u32_e32 v9, vcc, 0, v1, vcc
	s_nop 0
	v_cvt_pk_bf16_f32 v2, v76, v77
	v_cvt_pk_bf16_f32 v3, v78, v79
	v_cvt_pk_bf16_f32 v4, v72, v73
	v_cvt_pk_bf16_f32 v5, v74, v75
	v_lshl_add_u64 v[6:7], v[0:1], 0, s[20:21]
	global_store_dwordx4 v[8:9], v[2:5], off
	v_add_co_u32_e32 v8, vcc, s72, v0
	s_nop 0
	v_cvt_pk_bf16_f32 v2, v68, v69
	v_cvt_pk_bf16_f32 v3, v70, v71
	v_cvt_pk_bf16_f32 v4, v64, v65
	v_cvt_pk_bf16_f32 v5, v66, v67
	global_store_dwordx4 v[6:7], v[2:5], off offset:256
	v_lshl_add_u64 v[6:7], v[0:1], 0, s[22:23]
	v_addc_co_u32_e32 v9, vcc, 0, v1, vcc
	v_cvt_pk_bf16_f32 v2, v60, v61
	v_cvt_pk_bf16_f32 v3, v62, v63
	v_cvt_pk_bf16_f32 v4, v56, v57
	v_cvt_pk_bf16_f32 v5, v58, v59
	global_store_dwordx4 v[8:9], v[2:5], off
	s_nop 1
	v_cvt_pk_bf16_f32 v2, v52, v53
	v_cvt_pk_bf16_f32 v3, v54, v55
	v_cvt_pk_bf16_f32 v4, v48, v49
	v_cvt_pk_bf16_f32 v5, v50, v51
	global_store_dwordx4 v[6:7], v[2:5], off offset:256
	v_lshl_add_u64 v[6:7], v[0:1], 0, s[24:25]
	v_add_co_u32_e32 v0, vcc, s73, v0
	v_cvt_pk_bf16_f32 v2, v44, v45
	v_cvt_pk_bf16_f32 v3, v46, v47
	v_cvt_pk_bf16_f32 v4, v40, v41
	v_cvt_pk_bf16_f32 v5, v42, v43
	s_nop 1
	v_addc_co_u32_e32 v1, vcc, 0, v1, vcc
	s_and_b64 vcc, exec, s[0:1]
	s_mov_b64 s[0:1], -1
	global_store_dwordx4 v[0:1], v[2:5], off
	v_cvt_pk_bf16_f32 v0, v36, v37
	v_cvt_pk_bf16_f32 v1, v38, v39
	s_nop 1
	v_cvt_pk_bf16_f32 v2, v32, v33
	v_cvt_pk_bf16_f32 v3, v34, v35
	global_store_dwordx4 v[6:7], v[0:3], off offset:256
	s_cbranch_vccnz .LBB0_1441
	s_andn2_b64 vcc, exec, s[10:11]
	s_cbranch_vccnz .LBB0_1440
	s_barrier
	s_branch .LBB0_1440
